# P0 rmsnorm row loop: pointers via scalar loads before the loop, gamma chunks loaded together with the row, one wait per row
# speedup vs baseline: 1.0033x; 1.0018x over previous
; __device__ __forceinline__ void p0_prologue(const Ctx& C) {
;     ...
;     const int gw = C.bid * 8 + C.wave, NWV = C.G * 8, lane = C.lane;
;     for (int row = gw; row < T_ + NB * MEMT; row += NWV) {
;         const bool ismem = row >= T_; const float* src = ismem ? C.ka->in[I_MEM] + (size_t)(row - T_) * D_ : C.ka->in[I_X] + (size_t)row * D_;
;         const float* gv = ismem ? C.ka->in[I_MEMG] : C.ka->in[I_MIXG]; bf16_t* dst = WSP(bf16_t, WS_H) + (size_t)row * D_; unsigned char* d8 = ismem ? WSP(unsigned char, WS_MEMN) + (size_t)(row - T_) * D_ : WSP(unsigned char, WS_H8) + (size_t)row * D_;
.LBB0_75:
	v_readlane_b32 s0, v254, 0
	s_lshl_b32 s0, s0, 3
	s_add_i32 s2, s56, s0
	v_and_b32_e32 v1, 63, v30
	s_cmp_gt_i32 s2, 0x81ff
	s_barrier
	v_readlane_b32 s1, v254, 1
	s_cbranch_scc1 .LBB0_98
	v_readlane_b32 s0, v254, 2
	s_lshl_b32 s10, s0, 3
	s_add_u32 s24, s62, 0x70998800
	v_mov_b32_e32 v33, 0
	s_addc_u32 s25, s63, 0
	v_readlane_b32 s1, v254, 3
	s_waitcnt vmcnt(0)
	v_lshlrev_b32_e32 v2, 3, v1
	v_mov_b32_e32 v3, v33
	s_add_u32 s26, s62, 0x3a000800
	v_lshlrev_b32_e32 v32, 2, v1
	v_lshl_add_u64 v[2:3], s[62:63], 0, v[2:3]
	s_mov_b64 s[0:1], 0x10000
	s_addc_u32 s27, s63, 0
	s_ashr_i32 s3, s2, 31
	s_ashr_i32 s11, s10, 31
	v_lshl_add_u64 v[34:35], v[2:3], 0, s[0:1]
	s_lshl_b64 s[12:13], s[2:3], 13
	s_lshl_b64 s[14:15], s[10:11], 13
	s_mov_b32 s17, 0
	v_lshlrev_b32_e32 v36, 2, v32
	v_mov_b32_e32 v37, v33
	s_movk_i32 s28, 0x1000
	v_mov_b32_e32 v31, 0x358637bd
	s_mov_b32 s29, 0x800000
	s_mov_b32 s30, 0xc3e00000
	v_mov_b32_e32 v44, 0x43e00000
	s_load_dwordx2 s[84:85], s[34:35], 0x0
	s_load_dwordx2 s[86:87], s[34:35], 0x8
	s_load_dwordx2 s[88:89], s[34:35], 0x18
	s_load_dwordx2 s[90:91], s[34:35], 0x20
	s_waitcnt lgkmcnt(0)
	s_branch .LBB0_78

; __device__ __forceinline__ void p0_prologue(const Ctx& C) {
;     ...
;     for (int row = gw; row < T_ + NB * MEMT; row += NWV) {
;         const bool ismem = row >= T_; const float* src = ismem ? C.ka->in[I_MEM] + (size_t)(row - T_) * D_ : C.ka->in[I_X] + (size_t)row * D_;
;         const float* gv = ismem ? C.ka->in[I_MEMG] : C.ka->in[I_MIXG]; bf16_t* dst = WSP(bf16_t, WS_H) + (size_t)row * D_; unsigned char* d8 = ismem ? WSP(unsigned char, WS_MEMN) + (size_t)(row - T_) * D_ : WSP(unsigned char, WS_H8) + (size_t)row * D_;
.LBB0_78:
	s_cmpk_gt_i32 s2, 0x7fff
	s_cselect_b64 s[18:19], -1, 0
	s_cmp_lt_i32 s2, 0x8000
	s_cselect_b64 s[22:23], -1, 0
	s_and_b64 vcc, exec, s[22:23]
	s_cbranch_vccz .LBB0_80
	v_mov_b64_e32 v[2:3], s[84:85]
	s_mov_b64 s[92:93], s[88:89]
	s_add_i32 s16, s2, 0xffff8000
	s_mov_b64 s[20:21], s[2:3]
	s_nop 0
	v_lshl_add_u64 v[2:3], v[2:3], 0, s[12:13]
	s_mov_b64 s[0:1], 24
	s_cbranch_execz .LBB0_81
	s_branch .LBB0_82

; __device__ __forceinline__ unsigned cvt_pk_bf16(float lo, float hi) { unsigned r; asm volatile("v_cvt_pk_bf16_f32 %0, %1, %2" : "=v"(r) : "v"(lo), "v"(hi)); return r; }
; __device__ __forceinline__ void p0_prologue(const Ctx& C) {
;     ...
;     for (int row = gw; row < T_ + NB * MEMT; row += NWV) {
;         const bool ismem = row >= T_; const float* src = ismem ? C.ka->in[I_MEM] + (size_t)(row - T_) * D_ : C.ka->in[I_X] + (size_t)row * D_;
;         const float* gv = ismem ? C.ka->in[I_MEMG] : C.ka->in[I_MIXG]; bf16_t* dst = WSP(bf16_t, WS_H) + (size_t)row * D_; unsigned char* d8 = ismem ? WSP(unsigned char, WS_MEMN) + (size_t)(row - T_) * D_ : WSP(unsigned char, WS_H8) + (size_t)row * D_;
;         f32x4 v[8]; float ss = 0.f;
; #pragma unroll
;         for (int c = 0; c < 8; ++c) { v[c] = __builtin_nontemporal_load((const f32x4*)(src + c * 256 + lane * 4)); ss += (v[c][0] * v[c][0] + v[c][1] * v[c][1]) + (v[c][2] * v[c][2] + v[c][3] * v[c][3]); }
;         ss = wave_sum(ss); const float rs = rsqrtf(ss * (1.0f / D_) + EPS);
; #pragma unroll
;         for (int c = 0; c < 8; ++c) { const f32x4 g4 = *(const f32x4*)(gv + c * 256 + lane * 4); const float h0 = v[c][0] * rs * g4[0], h1 = v[c][1] * rs * g4[1], h2 = v[c][2] * rs * g4[2], h3 = v[c][3] * rs * g4[3];
;             if (!ismem) { u32x2 w; w.x = cvt_pk_bf16(h0, h1); w.y = cvt_pk_bf16(h2, h3); *(u32x2*)(dst + c * 256 + lane * 4) = w; }
.LBB0_81:
	v_mov_b64_e32 v[2:3], s[86:87]
	s_mov_b64 s[92:93], s[90:91]
	s_add_i32 s16, s2, 0xffff8000
	s_lshl_b64 s[0:1], s[16:17], 13
	s_nop 0
	v_lshl_add_u64 v[2:3], v[2:3], 0, s[0:1]
	s_mov_b64 s[0:1], 32
.LBB0_82:
	s_mov_b64 s[6:7], s[34:35]
	s_add_u32 s0, s6, s0
	s_addc_u32 s1, s7, s1
	v_lshl_add_u64 v[2:3], v[2:3], 0, v[36:37]
	v_mov_b64_e32 v[4:5], s[0:1]
	global_load_dwordx4 v[46:49], v[2:3], off nt
	global_load_dwordx4 v[26:29], v[2:3], off offset:1024 nt
	v_lshl_add_u64 v[38:39], s[92:93], 0, v[36:37]
	global_load_dwordx4 v[22:25], v[2:3], off offset:2048 nt
	global_load_dwordx4 v[18:21], v[2:3], off offset:3072 nt
	v_add_co_u32_e32 v40, vcc, s28, v2
	v_cndmask_b32_e64 v45, 0, 1, s[22:23]
	s_nop 0
	v_addc_co_u32_e32 v41, vcc, 0, v3, vcc
	global_load_dwordx4 v[10:13], v[40:41], off offset:1024 nt
	global_load_dwordx4 v[14:17], v[40:41], off nt
	global_load_dwordx4 v[2:5], v[40:41], off offset:3072 nt
	global_load_dwordx4 v[6:9], v[40:41], off offset:2048 nt
	v_add_co_u32_e32 v232, vcc, s28, v38
	s_nop 1
	v_addc_co_u32_e32 v233, vcc, 0, v39, vcc
	global_load_dwordx4 v[200:203], v[38:39], off
	global_load_dwordx4 v[204:207], v[38:39], off offset:1024
	global_load_dwordx4 v[208:211], v[38:39], off offset:2048
	global_load_dwordx4 v[212:215], v[38:39], off offset:3072
	global_load_dwordx4 v[216:219], v[232:233], off
	global_load_dwordx4 v[220:223], v[232:233], off offset:1024
	global_load_dwordx4 v[224:227], v[232:233], off offset:2048
	global_load_dwordx4 v[228:231], v[232:233], off offset:3072
	s_lshl_b64 s[0:1], s[20:21], 12
	s_andn2_b64 vcc, exec, s[22:23]
	s_waitcnt vmcnt(0) lgkmcnt(0)
	v_mov_b32_e32 v42, v47
	s_nop 0
	s_nop 0
	v_mov_b32_e32 v43, v27
	v_mov_b32_e32 v56, v49
	v_mov_b32_e32 v57, v29
	v_mov_b32_e32 v40, v46
	v_mov_b32_e32 v41, v26
	v_mov_b32_e32 v54, v48
	v_mov_b32_e32 v55, v28
	v_pk_mul_f32 v[58:59], v[24:25], v[24:25]
	v_pk_mul_f32 v[60:61], v[22:23], v[22:23]
	v_pk_mul_f32 v[42:43], v[42:43], v[42:43]
	v_pk_mul_f32 v[56:57], v[56:57], v[56:57]
	v_pk_mov_b32 v[66:67], v[60:61], v[58:59] op_sel:[1,0]
	v_mov_b32_e32 v61, v59
	v_pk_fma_f32 v[40:41], v[40:41], v[40:41], v[42:43]
	v_pk_fma_f32 v[42:43], v[54:55], v[54:55], v[56:57]
	v_mul_f32_e32 v62, v19, v19
	v_mul_f32_e32 v64, v21, v21
	v_pk_add_f32 v[54:55], v[66:67], v[60:61]
	v_pk_add_f32 v[40:41], v[40:41], v[42:43]
	v_mul_f32_e32 v71, v14, v14
	v_mul_f32_e32 v73, v15, v15
	v_mul_f32_e32 v74, v16, v16
	v_mul_f32_e32 v75, v17, v17
	v_pk_fma_f32 v[62:63], v[18:19], v[18:19], v[62:63] op_sel_hi:[1,1,0]
	v_pk_fma_f32 v[64:65], v[20:21], v[20:21], v[64:65] op_sel_hi:[1,1,0]
	v_pk_add_f32 v[54:55], v[54:55], v[54:55] op_sel:[0,1] op_sel_hi:[1,0]
	v_pk_add_f32 v[40:41], v[40:41], v[40:41] op_sel:[0,1] op_sel_hi:[1,0]
	v_pk_mul_f32 v[58:59], v[12:13], v[12:13]
	v_pk_mul_f32 v[68:69], v[10:11], v[10:11]
	v_mov_b32_e32 v63, v74
	v_mov_b32_e32 v65, v75
	v_mov_b32_e32 v55, v73
	v_mov_b32_e32 v41, v71
	v_pk_mov_b32 v[56:57], v[68:69], v[58:59] op_sel:[1,0]
	v_mov_b32_e32 v69, v59
	v_pk_add_f32 v[42:43], v[62:63], v[64:65]
	v_pk_add_f32 v[40:41], v[40:41], v[54:55]
	v_mul_f32_e32 v70, v7, v7
	v_mul_f32_e32 v72, v9, v9
	v_pk_add_f32 v[56:57], v[56:57], v[68:69]
	v_pk_add_f32 v[40:41], v[40:41], v[42:43]
	v_mul_f32_e32 v76, v2, v2
	v_mul_f32_e32 v77, v4, v4
	v_mul_f32_e32 v78, v5, v5
	v_mul_f32_e32 v79, v3, v3
	v_pk_fma_f32 v[58:59], v[6:7], v[6:7], v[70:71] op_sel_hi:[1,1,0]
	v_pk_fma_f32 v[60:61], v[8:9], v[8:9], v[72:73] op_sel_hi:[1,1,0]
	v_pk_add_f32 v[56:57], v[56:57], v[56:57] op_sel:[0,1] op_sel_hi:[1,0]
	v_pk_add_f32 v[40:41], v[40:41], v[40:41] op_sel:[0,1] op_sel_hi:[1,0]
	v_mov_b32_e32 v59, v77
	v_mov_b32_e32 v61, v78
	v_mov_b32_e32 v57, v79
	v_mov_b32_e32 v41, v76
	v_pk_add_f32 v[58:59], v[58:59], v[60:61]
	v_pk_add_f32 v[40:41], v[40:41], v[56:57]
	s_nop 0
	v_pk_add_f32 v[40:41], v[40:41], v[58:59]
	s_nop 0
	v_add_f32_e32 v40, v40, v41
	s_nop 1
	v_add_f32_dpp v40, v40, v40 quad_perm:[1,0,3,2] row_mask:0xf bank_mask:0xf bound_ctrl:1
	s_nop 1
	v_add_f32_dpp v40, v40, v40 quad_perm:[2,3,0,1] row_mask:0xf bank_mask:0xf bound_ctrl:1
	s_nop 1
	v_add_f32_dpp v40, v40, v40 row_half_mirror row_mask:0xf bank_mask:0xf bound_ctrl:1
	s_nop 1
	v_add_f32_dpp v40, v40, v40 row_mirror row_mask:0xf bank_mask:0xf bound_ctrl:1
	s_nop 0
	v_readlane_b32 s8, v40, 16
	v_readlane_b32 s9, v40, 48
	v_readlane_b32 s6, v40, 0
	v_readlane_b32 s7, v40, 32
	v_mov_b32_e32 v40, s8
	v_mov_b32_e32 v41, s9
	v_pk_add_f32 v[40:41], s[6:7], v[40:41]
	v_cmp_ne_u32_e64 s[6:7], 1, v45
	v_add_f32_e32 v40, v40, v41
	v_fmamk_f32 v40, v40, 0x3a000000, v31
	v_mul_f32_e32 v41, 0x4b800000, v40
	v_cmp_gt_f32_e64 s[8:9], s29, v40
	s_nop 1
	v_cndmask_b32_e64 v40, v40, v41, s[8:9]
	v_rsq_f32_e32 v42, v40
	v_lshl_add_u64 v[40:41], v[34:35], 0, s[0:1]
	v_mul_f32_e32 v43, 0x45800000, v42
	v_cndmask_b32_e64 v45, v42, v43, s[8:9]
	v_mul_f32_e32 v42, v46, v45
	v_mul_f32_e32 v43, v47, v45
	v_mul_f32_e32 v48, v48, v45
	v_mul_f32_e32 v49, v49, v45
	s_waitcnt vmcnt(0) lgkmcnt(0)
	v_mul_f32_e32 v47, v200, v42
	v_mul_f32_e32 v46, v201, v43
	v_mul_f32_e32 v43, v202, v48
	v_mul_f32_e32 v42, v203, v49
	s_cbranch_vccnz .LBB0_84
	v_cvt_pk_bf16_f32 v48, v47, v46
	v_cvt_pk_bf16_f32 v49, v43, v42
	global_store_dwordx2 v[40:41], v[48:49], off
; __device__ __forceinline__ unsigned cvt_pk_bf16(float lo, float hi) { unsigned r; asm volatile("v_cvt_pk_bf16_f32 %0, %1, %2" : "=v"(r) : "v"(lo), "v"(hi)); return r; }
; __device__ __forceinline__ void p0_prologue(const Ctx& C) {
;     ...
; #pragma unroll
;         for (int c = 0; c < 8; ++c) { const f32x4 g4 = *(const f32x4*)(gv + c * 256 + lane * 4); const float h0 = v[c][0] * rs * g4[0], h1 = v[c][1] * rs * g4[1], h2 = v[c][2] * rs * g4[2], h3 = v[c][3] * rs * g4[3];
;             if (!ismem) { u32x2 w; w.x = cvt_pk_bf16(h0, h1); w.y = cvt_pk_bf16(h2, h3); *(u32x2*)(dst + c * 256 + lane * 4) = w; }
;             *(unsigned*)(d8 + c * 256 + lane * 4) = pk4_fp8(h0, h1, h2, h3); }
.LBB0_84:
	v_max_f32_e32 v47, v47, v47
	v_max_f32_e32 v46, v46, v46
	v_med3_f32 v47, v47, s30, v44
	v_med3_f32 v46, v46, s30, v44
	s_lshl_b64 s[0:1], s[20:21], 11
	s_lshl_b64 s[8:9], s[16:17], 11
	v_cvt_pk_fp8_f32 v48, v47, v46
	s_add_u32 s8, s26, s8
	s_addc_u32 s9, s27, s9
	v_max_f32_e32 v43, v43, v43
	v_max_f32_e32 v42, v42, v42
	s_add_u32 s16, s24, s0
	v_med3_f32 v43, v43, s30, v44
	v_med3_f32 v42, v42, s30, v44
	s_addc_u32 s20, s25, s1
	v_cvt_pk_fp8_f32 v48, v43, v42 op_sel:[0,0,1]
	s_and_b64 s[0:1], s[18:19], exec
	s_cselect_b32 s1, s9, s20
	s_cselect_b32 s0, s8, s16
	v_lshl_add_u64 v[42:43], s[0:1], 0, v[32:33]
	global_store_dword v[42:43], v48, off
	s_nop 0
	v_mul_f32_e32 v26, v26, v45
	v_mul_f32_e32 v27, v27, v45
	v_mul_f32_e32 v50, v28, v45
	v_mul_f32_e32 v51, v29, v45
	s_and_b64 vcc, exec, s[6:7]
	s_nop 0
	v_mul_f32_e32 v29, v26, v204
	v_mul_f32_e32 v28, v27, v205
	v_mul_f32_e32 v27, v50, v206
	v_mul_f32_e32 v26, v51, v207
	s_cbranch_vccnz .LBB0_86
	v_cvt_pk_bf16_f32 v46, v29, v28
	v_cvt_pk_bf16_f32 v47, v27, v26
	global_store_dwordx2 v[40:41], v[46:47], off offset:512
.LBB0_86:
	v_max_f32_e32 v29, v29, v29
	v_max_f32_e32 v28, v28, v28
	v_med3_f32 v29, v29, s30, v44
	v_med3_f32 v28, v28, s30, v44
	v_cvt_pk_fp8_f32 v46, v29, v28
	v_max_f32_e32 v27, v27, v27
	v_max_f32_e32 v26, v26, v26
	v_med3_f32 v27, v27, s30, v44
	v_med3_f32 v26, v26, s30, v44
	v_cvt_pk_fp8_f32 v46, v27, v26 op_sel:[0,0,1]
	v_mul_f32_e32 v22, v22, v45
	v_mul_f32_e32 v23, v23, v45
	v_mul_f32_e32 v47, v25, v45
	global_store_dword v[42:43], v46, off offset:256
	s_nop 0
	v_mul_f32_e32 v46, v24, v45
	s_and_b64 vcc, exec, s[6:7]
	s_nop 0
	v_mul_f32_e32 v25, v22, v208
	v_mul_f32_e32 v24, v23, v209
	v_mul_f32_e32 v23, v46, v210
	v_mul_f32_e32 v22, v47, v211
	s_cbranch_vccnz .LBB0_88
	v_cvt_pk_bf16_f32 v26, v25, v24
	v_cvt_pk_bf16_f32 v27, v23, v22
	global_store_dwordx2 v[40:41], v[26:27], off offset:1024
.LBB0_88:
	v_max_f32_e32 v25, v25, v25
	v_max_f32_e32 v24, v24, v24
	v_med3_f32 v25, v25, s30, v44
	v_med3_f32 v24, v24, s30, v44
	v_cvt_pk_fp8_f32 v26, v25, v24
	v_max_f32_e32 v23, v23, v23
	v_max_f32_e32 v22, v22, v22
	v_med3_f32 v23, v23, s30, v44
	v_med3_f32 v22, v22, s30, v44
	v_cvt_pk_fp8_f32 v26, v23, v22 op_sel:[0,0,1]
	v_mul_f32_e32 v18, v18, v45
	v_mul_f32_e32 v19, v19, v45
	v_mul_f32_e32 v27, v21, v45
	global_store_dword v[42:43], v26, off offset:512
	s_nop 0
	v_mul_f32_e32 v26, v20, v45
	s_and_b64 vcc, exec, s[6:7]
	s_nop 0
	v_mul_f32_e32 v21, v18, v212
	v_mul_f32_e32 v20, v19, v213
	v_mul_f32_e32 v19, v26, v214
	v_mul_f32_e32 v18, v27, v215
	s_cbranch_vccnz .LBB0_90
	v_cvt_pk_bf16_f32 v22, v21, v20
	v_cvt_pk_bf16_f32 v23, v19, v18
	global_store_dwordx2 v[40:41], v[22:23], off offset:1536
.LBB0_90:
	v_max_f32_e32 v21, v21, v21
	v_max_f32_e32 v20, v20, v20
	v_med3_f32 v21, v21, s30, v44
	v_med3_f32 v20, v20, s30, v44
	v_cvt_pk_fp8_f32 v22, v21, v20
	v_max_f32_e32 v19, v19, v19
	v_max_f32_e32 v18, v18, v18
	v_med3_f32 v19, v19, s30, v44
	v_med3_f32 v18, v18, s30, v44
	v_cvt_pk_fp8_f32 v22, v19, v18 op_sel:[0,0,1]
	v_add_co_u32_e32 v18, vcc, 0x1000, v38
	v_mul_f32_e32 v14, v14, v45
	global_store_dword v[42:43], v22, off offset:768
	v_addc_co_u32_e32 v19, vcc, 0, v39, vcc
	s_nop 0
	v_mul_f32_e32 v15, v15, v45
	v_mul_f32_e32 v22, v16, v45
	v_mul_f32_e32 v23, v17, v45
	s_and_b64 vcc, exec, s[6:7]
	s_nop 0
	v_mul_f32_e32 v17, v14, v216
	v_mul_f32_e32 v16, v15, v217
	v_mul_f32_e32 v15, v22, v218
	v_mul_f32_e32 v14, v23, v219
	s_cbranch_vccnz .LBB0_92
	v_cvt_pk_bf16_f32 v18, v17, v16
	v_cvt_pk_bf16_f32 v19, v15, v14
	global_store_dwordx2 v[40:41], v[18:19], off offset:2048
.LBB0_92:
	v_max_f32_e32 v17, v17, v17
	v_max_f32_e32 v16, v16, v16
	v_med3_f32 v17, v17, s30, v44
	v_med3_f32 v16, v16, s30, v44
	v_cvt_pk_fp8_f32 v18, v17, v16
	v_max_f32_e32 v15, v15, v15
	v_max_f32_e32 v14, v14, v14
	v_med3_f32 v15, v15, s30, v44
	v_med3_f32 v14, v14, s30, v44
	v_cvt_pk_fp8_f32 v18, v15, v14 op_sel:[0,0,1]
	v_add_co_u32_e32 v14, vcc, s28, v38
	v_mul_f32_e32 v10, v10, v45
	global_store_dword v[42:43], v18, off offset:1024
	v_addc_co_u32_e32 v15, vcc, 0, v39, vcc
	s_nop 0
	v_mul_f32_e32 v11, v11, v45
	v_mul_f32_e32 v20, v12, v45
	v_mul_f32_e32 v21, v13, v45
	s_and_b64 vcc, exec, s[6:7]
	s_nop 0
	v_mul_f32_e32 v13, v10, v220
	v_mul_f32_e32 v12, v11, v221
	v_mul_f32_e32 v11, v20, v222
	v_mul_f32_e32 v10, v21, v223
	s_cbranch_vccnz .LBB0_94
	v_cvt_pk_bf16_f32 v16, v13, v12
	v_cvt_pk_bf16_f32 v17, v11, v10
	global_store_dwordx2 v[40:41], v[16:17], off offset:2560
.LBB0_94:
	v_max_f32_e32 v13, v13, v13
	v_max_f32_e32 v12, v12, v12
	v_med3_f32 v13, v13, s30, v44
	v_med3_f32 v12, v12, s30, v44
	v_cvt_pk_fp8_f32 v16, v13, v12
	v_max_f32_e32 v11, v11, v11
	v_max_f32_e32 v10, v10, v10
	v_med3_f32 v11, v11, s30, v44
	v_med3_f32 v10, v10, s30, v44
	v_cvt_pk_fp8_f32 v16, v11, v10 op_sel:[0,0,1]
	v_mul_f32_e32 v6, v6, v45
	v_mul_f32_e32 v7, v7, v45
	s_and_b64 vcc, exec, s[6:7]
	global_store_dword v[42:43], v16, off offset:1280
	s_nop 0
	v_mul_f32_e32 v14, v8, v45
	v_mul_f32_e32 v15, v9, v45
	s_nop 0
	v_mul_f32_e32 v9, v6, v224
	v_mul_f32_e32 v8, v7, v225
	v_mul_f32_e32 v7, v14, v226
	v_mul_f32_e32 v6, v15, v227
	s_cbranch_vccnz .LBB0_96
	v_cvt_pk_bf16_f32 v10, v9, v8
	v_cvt_pk_bf16_f32 v11, v7, v6
	global_store_dwordx2 v[40:41], v[10:11], off offset:3072
.LBB0_96:
	v_max_f32_e32 v9, v9, v9
	v_max_f32_e32 v8, v8, v8
	v_med3_f32 v9, v9, s30, v44
	v_med3_f32 v8, v8, s30, v44
	v_cvt_pk_fp8_f32 v10, v9, v8
	v_max_f32_e32 v7, v7, v7
	v_max_f32_e32 v6, v6, v6
	v_med3_f32 v7, v7, s30, v44
	v_med3_f32 v6, v6, s30, v44
	v_cvt_pk_fp8_f32 v10, v7, v6 op_sel:[0,0,1]
	v_add_co_u32_e32 v6, vcc, 0x1000, v38
	v_mul_f32_e32 v2, v2, v45
	global_store_dword v[42:43], v10, off offset:1536
	v_addc_co_u32_e32 v7, vcc, 0, v39, vcc
	s_nop 0
	v_mul_f32_e32 v3, v3, v45
	v_mul_f32_e32 v10, v4, v45
	v_mul_f32_e32 v11, v5, v45
	s_and_b64 vcc, exec, s[6:7]
	s_nop 0
	v_mul_f32_e32 v5, v2, v228
	v_mul_f32_e32 v4, v3, v229
	v_mul_f32_e32 v3, v10, v230
	v_mul_f32_e32 v2, v11, v231
	s_cbranch_vccnz .LBB0_77
	v_cvt_pk_bf16_f32 v6, v5, v4
	v_cvt_pk_bf16_f32 v7, v3, v2
	global_store_dwordx2 v[40:41], v[6:7], off offset:3584
	s_branch .LBB0_77
